# MoE-down GEMM: alignment barrier of the leading wave group moved from the head of its epilogue to its tail (epilogue runs under the trailing group's last MMA)
# speedup vs baseline: 1.0088x; 1.0088x over previous
; __device__ __forceinline__ unsigned cvt4_fp8(float a, float b, float c, float d) { int w = 0; w = __builtin_amdgcn_cvt_pk_fp8_f32(a, b, w, false); w = __builtin_amdgcn_cvt_pk_fp8_f32(c, d, w, true); return (unsigned)w; }
; #define PG8_BAR __builtin_amdgcn_s_barrier()
; template <class Epi, class Sched, bool GATHER, bool ALIGN_EPI, bool SP2, bool FP8>
; __device__ __forceinline__ void gemm_phase(LAS unsigned char* lds, const Gemm g, const Sched& S, const Epi& E) {
;     ...
;         if constexpr (ALIGN_EPI) { if (wr == 0) PG8_BAR; }
;         {
;             asm volatile("s_nop 15\n\ts_nop 3" : "+v"(acc[0][0][0][0]), "+v"(acc[0][0][0][1]), "+v"(acc[0][0][1][0]), "+v"(acc[0][0][1][1]), "+v"(acc[0][0][2][0]), "+v"(acc[0][0][2][1]), "+v"(acc[0][0][3][0]), "+v"(acc[0][0][3][1]));
;             asm volatile("" : "+v"(acc[0][1][0][0]), "+v"(acc[0][1][0][1]), "+v"(acc[0][1][1][0]), "+v"(acc[0][1][1][1]), "+v"(acc[0][1][2][0]), "+v"(acc[0][1][2][1]), "+v"(acc[0][1][3][0]), "+v"(acc[0][1][3][1]));
;             asm volatile("" : "+v"(acc[1][0][0][0]), "+v"(acc[1][0][0][1]), "+v"(acc[1][0][1][0]), "+v"(acc[1][0][1][1]), "+v"(acc[1][0][2][0]), "+v"(acc[1][0][2][1]), "+v"(acc[1][0][3][0]), "+v"(acc[1][0][3][1]));
;             asm volatile("" : "+v"(acc[1][1][0][0]), "+v"(acc[1][1][0][1]), "+v"(acc[1][1][1][0]), "+v"(acc[1][1][1][1]), "+v"(acc[1][1][2][0]), "+v"(acc[1][1][2][1]), "+v"(acc[1][1][3][0]), "+v"(acc[1][1][3][1]));
;         }
;     __device__ __forceinline__ void operator()(const f32x4 (&acc)[2][2][4][2], const pg8::Unit& u, const Pre& pre, int wr, int wc, int fr, int fq) const {
;         const int e = u.e, cn = u.pn - e * 8, col0 = cn * 256 + wc * 32 + 8 * fq;
;         f32x4 bv[2][2];
; #pragma unroll
;         for (int bj = 0; bj < 2; ++bj) { bv[bj][0] = pre.bv[bj][0]; bv[bj][1] = pre.bv[bj][1]; }
; #pragma unroll
;         for (int ai = 0; ai < 2; ++ai)
; #pragma unroll
;             for (int m = 0; m < 4; ++m) { unsigned char* rowp = YS + (size_t)(u.pm * 256 + ai * 128 + wr * 64 + m * 16 + fr) * DM + col0;
; #pragma unroll
;                 for (int bj = 0; bj < 2; ++bj) { const f32x4 v0 = acc[ai][bj][m][0] * 0.015625f + bv[bj][0], v1 = acc[ai][bj][m][1] * 0.015625f + bv[bj][1];
;                     u32x2 w; w.x = cvt4_fp8(v0[0], v0[1], v0[2], v0[3]); w.y = cvt4_fp8(v1[0], v1[1], v1[2], v1[3]);
;                     *(u32x2*)(rowp + bj * 128) = w; } }
.LBB0_1008:
.LBB0_1010:
	s_nop 15
	s_nop 3
	s_waitcnt vmcnt(18)
	v_pk_fma_f32 v[8:9], v[158:159], s[18:19], v[26:27] op_sel_hi:[1,0,1]
	v_pk_fma_f32 v[10:11], v[154:155], s[18:19], v[22:23] op_sel_hi:[1,0,1]
	v_cvt_pk_fp8_f32 v12, v8, v9
	v_cvt_pk_fp8_f32 v13, v10, v11
	v_mov_b32_e32 v3, v0
	v_pk_fma_f32 v[8:9], v[160:161], s[18:19], v[28:29] op_sel_hi:[1,0,1]
	v_readfirstlane_b32 s10, v3
	v_pk_fma_f32 v[10:11], v[156:157], s[18:19], v[24:25] op_sel_hi:[1,0,1]
	s_lshr_b32 s33, s10, 1
	s_ashr_i32 s10, s10, 2
	v_cvt_pk_fp8_f32 v12, v8, v9 op_sel:[0,0,1]
	v_cvt_pk_fp8_f32 v13, v10, v11 op_sel:[0,0,1]
	s_waitcnt vmcnt(16)
	v_pk_fma_f32 v[8:9], v[150:151], s[18:19], v[30:31] op_sel_hi:[1,0,1]
	v_pk_fma_f32 v[10:11], v[146:147], s[18:19], v[18:19] op_sel_hi:[1,0,1]
	s_andn2_b32 s10, s10, 63
	v_cvt_pk_fp8_f32 v14, v8, v9
	v_cvt_pk_fp8_f32 v15, v10, v11
	s_lshl_b32 s11, s65, 8
	s_lshl_b32 s65, s66, 11
	v_and_or_b32 v4, v3, 15, s10
	s_and_b32 s33, s33, 0x60
	s_sub_i32 s11, s11, s65
	v_lshl_add_u32 v4, s62, 8, v4
	v_lshrrev_b32_e32 v2, 1, v3
	s_or_b32 s11, s33, s11
	v_ashrrev_i32_e32 v5, 31, v4
	v_pk_fma_f32 v[8:9], v[152:153], s[18:19], v[32:33] op_sel_hi:[1,0,1]
	v_pk_fma_f32 v[10:11], v[148:149], s[18:19], v[20:21] op_sel_hi:[1,0,1]
	v_and_or_b32 v2, v2, 24, s11
	v_lshlrev_b64 v[6:7], 11, v[4:5]
	v_cvt_pk_fp8_f32 v14, v8, v9 op_sel:[0,0,1]
	v_cvt_pk_fp8_f32 v15, v10, v11 op_sel:[0,0,1]
	v_ashrrev_i32_e32 v3, 31, v2
	v_lshl_add_u64 v[6:7], s[14:15], 0, v[6:7]
	v_lshl_add_u64 v[6:7], v[6:7], 0, v[2:3]
	global_store_dwordx2 v[6:7], v[12:13], off
	global_store_dwordx2 v[6:7], v[14:15], off offset:128
	v_pk_fma_f32 v[8:9], v[142:143], s[18:19], v[26:27] op_sel_hi:[1,0,1]
	v_pk_fma_f32 v[10:11], v[138:139], s[18:19], v[22:23] op_sel_hi:[1,0,1]
	v_cvt_pk_fp8_f32 v12, v8, v9
	v_cvt_pk_fp8_f32 v13, v10, v11
	v_pk_fma_f32 v[8:9], v[144:145], s[18:19], v[28:29] op_sel_hi:[1,0,1]
	v_pk_fma_f32 v[10:11], v[140:141], s[18:19], v[24:25] op_sel_hi:[1,0,1]
	v_cvt_pk_fp8_f32 v12, v8, v9 op_sel:[0,0,1]
	v_cvt_pk_fp8_f32 v13, v10, v11 op_sel:[0,0,1]
	v_pk_fma_f32 v[8:9], v[134:135], s[18:19], v[30:31] op_sel_hi:[1,0,1]
	v_pk_fma_f32 v[10:11], v[130:131], s[18:19], v[18:19] op_sel_hi:[1,0,1]
	v_cvt_pk_fp8_f32 v14, v8, v9
	v_cvt_pk_fp8_f32 v15, v10, v11
	v_or_b32_e32 v6, 16, v4
	v_ashrrev_i32_e32 v7, 31, v6
	v_pk_fma_f32 v[8:9], v[136:137], s[18:19], v[32:33] op_sel_hi:[1,0,1]
	v_pk_fma_f32 v[10:11], v[132:133], s[18:19], v[20:21] op_sel_hi:[1,0,1]
	v_lshlrev_b64 v[6:7], 11, v[6:7]
	v_cvt_pk_fp8_f32 v14, v8, v9 op_sel:[0,0,1]
	v_cvt_pk_fp8_f32 v15, v10, v11 op_sel:[0,0,1]
	v_lshl_add_u64 v[6:7], s[14:15], 0, v[6:7]
	v_lshl_add_u64 v[6:7], v[6:7], 0, v[2:3]
	global_store_dwordx2 v[6:7], v[12:13], off
	global_store_dwordx2 v[6:7], v[14:15], off offset:128
	v_pk_fma_f32 v[8:9], v[126:127], s[18:19], v[26:27] op_sel_hi:[1,0,1]
	v_pk_fma_f32 v[10:11], v[122:123], s[18:19], v[22:23] op_sel_hi:[1,0,1]
	v_cvt_pk_fp8_f32 v12, v8, v9
	v_cvt_pk_fp8_f32 v13, v10, v11
	v_pk_fma_f32 v[8:9], v[128:129], s[18:19], v[28:29] op_sel_hi:[1,0,1]
	v_pk_fma_f32 v[10:11], v[124:125], s[18:19], v[24:25] op_sel_hi:[1,0,1]
	v_cvt_pk_fp8_f32 v12, v8, v9 op_sel:[0,0,1]
	v_cvt_pk_fp8_f32 v13, v10, v11 op_sel:[0,0,1]
	v_pk_fma_f32 v[8:9], v[118:119], s[18:19], v[30:31] op_sel_hi:[1,0,1]
	v_pk_fma_f32 v[10:11], v[114:115], s[18:19], v[18:19] op_sel_hi:[1,0,1]
	v_cvt_pk_fp8_f32 v14, v8, v9
	v_cvt_pk_fp8_f32 v15, v10, v11
	v_or_b32_e32 v6, 32, v4
	v_ashrrev_i32_e32 v7, 31, v6
	v_pk_fma_f32 v[8:9], v[120:121], s[18:19], v[32:33] op_sel_hi:[1,0,1]
	v_pk_fma_f32 v[10:11], v[116:117], s[18:19], v[20:21] op_sel_hi:[1,0,1]
	v_lshlrev_b64 v[6:7], 11, v[6:7]
	v_cvt_pk_fp8_f32 v14, v8, v9 op_sel:[0,0,1]
	v_cvt_pk_fp8_f32 v15, v10, v11 op_sel:[0,0,1]
	v_lshl_add_u64 v[6:7], s[14:15], 0, v[6:7]
	v_lshl_add_u64 v[6:7], v[6:7], 0, v[2:3]
	global_store_dwordx2 v[6:7], v[12:13], off
	global_store_dwordx2 v[6:7], v[14:15], off offset:128
	v_pk_fma_f32 v[8:9], v[110:111], s[18:19], v[26:27] op_sel_hi:[1,0,1]
	v_pk_fma_f32 v[10:11], v[106:107], s[18:19], v[22:23] op_sel_hi:[1,0,1]
	v_cvt_pk_fp8_f32 v12, v8, v9
	v_cvt_pk_fp8_f32 v13, v10, v11
	v_pk_fma_f32 v[8:9], v[112:113], s[18:19], v[28:29] op_sel_hi:[1,0,1]
	v_pk_fma_f32 v[10:11], v[108:109], s[18:19], v[24:25] op_sel_hi:[1,0,1]
	v_cvt_pk_fp8_f32 v12, v8, v9 op_sel:[0,0,1]
	v_cvt_pk_fp8_f32 v13, v10, v11 op_sel:[0,0,1]
	v_pk_fma_f32 v[8:9], v[102:103], s[18:19], v[30:31] op_sel_hi:[1,0,1]
	v_pk_fma_f32 v[10:11], v[98:99], s[18:19], v[18:19] op_sel_hi:[1,0,1]
	v_cvt_pk_fp8_f32 v14, v8, v9
	v_cvt_pk_fp8_f32 v15, v10, v11
	v_or_b32_e32 v6, 48, v4
	v_ashrrev_i32_e32 v7, 31, v6
	v_pk_fma_f32 v[8:9], v[104:105], s[18:19], v[32:33] op_sel_hi:[1,0,1]
	v_pk_fma_f32 v[10:11], v[100:101], s[18:19], v[20:21] op_sel_hi:[1,0,1]
	v_lshlrev_b64 v[6:7], 11, v[6:7]
	v_cvt_pk_fp8_f32 v14, v8, v9 op_sel:[0,0,1]
	v_cvt_pk_fp8_f32 v15, v10, v11 op_sel:[0,0,1]
	v_lshl_add_u64 v[6:7], s[14:15], 0, v[6:7]
; __device__ __forceinline__ unsigned cvt4_fp8(float a, float b, float c, float d) { int w = 0; w = __builtin_amdgcn_cvt_pk_fp8_f32(a, b, w, false); w = __builtin_amdgcn_cvt_pk_fp8_f32(c, d, w, true); return (unsigned)w; }
; #define PG8_BAR __builtin_amdgcn_s_barrier()
; template <class Epi, class Sched, bool GATHER, bool ALIGN_EPI, bool SP2, bool FP8>
; __device__ __forceinline__ void gemm_phase(LAS unsigned char* lds, const Gemm g, const Sched& S, const Epi& E) {
;     ...
;         if constexpr (ALIGN_EPI) { if (wr == 0) PG8_BAR; }
;     __device__ __forceinline__ void operator()(const f32x4 (&acc)[2][2][4][2], const pg8::Unit& u, const Pre& pre, int wr, int wc, int fr, int fq) const {
;     ...
;         for (int ai = 0; ai < 2; ++ai)
; #pragma unroll
;             for (int m = 0; m < 4; ++m) { unsigned char* rowp = YS + (size_t)(u.pm * 256 + ai * 128 + wr * 64 + m * 16 + fr) * DM + col0;
; #pragma unroll
;                 for (int bj = 0; bj < 2; ++bj) { const f32x4 v0 = acc[ai][bj][m][0] * 0.015625f + bv[bj][0], v1 = acc[ai][bj][m][1] * 0.015625f + bv[bj][1];
;                     u32x2 w; w.x = cvt4_fp8(v0[0], v0[1], v0[2], v0[3]); w.y = cvt4_fp8(v1[0], v1[1], v1[2], v1[3]);
;                     *(u32x2*)(rowp + bj * 128) = w; } }
	v_lshl_add_u64 v[6:7], v[6:7], 0, v[2:3]
	global_store_dwordx2 v[6:7], v[12:13], off
	global_store_dwordx2 v[6:7], v[14:15], off offset:128
	v_pk_fma_f32 v[8:9], v[94:95], s[18:19], v[26:27] op_sel_hi:[1,0,1]
	v_pk_fma_f32 v[10:11], v[90:91], s[18:19], v[22:23] op_sel_hi:[1,0,1]
	v_cvt_pk_fp8_f32 v12, v8, v9
	v_cvt_pk_fp8_f32 v13, v10, v11
	v_pk_fma_f32 v[8:9], v[96:97], s[18:19], v[28:29] op_sel_hi:[1,0,1]
	v_pk_fma_f32 v[10:11], v[92:93], s[18:19], v[24:25] op_sel_hi:[1,0,1]
	v_cvt_pk_fp8_f32 v12, v8, v9 op_sel:[0,0,1]
	v_cvt_pk_fp8_f32 v13, v10, v11 op_sel:[0,0,1]
	v_pk_fma_f32 v[8:9], v[86:87], s[18:19], v[30:31] op_sel_hi:[1,0,1]
	v_pk_fma_f32 v[10:11], v[82:83], s[18:19], v[18:19] op_sel_hi:[1,0,1]
	v_cvt_pk_fp8_f32 v14, v8, v9
	v_cvt_pk_fp8_f32 v15, v10, v11
	v_add_u32_e32 v6, 0x80, v4
	v_ashrrev_i32_e32 v7, 31, v6
	v_pk_fma_f32 v[8:9], v[88:89], s[18:19], v[32:33] op_sel_hi:[1,0,1]
	v_pk_fma_f32 v[10:11], v[84:85], s[18:19], v[20:21] op_sel_hi:[1,0,1]
	v_lshlrev_b64 v[6:7], 11, v[6:7]
	v_cvt_pk_fp8_f32 v14, v8, v9 op_sel:[0,0,1]
	v_cvt_pk_fp8_f32 v15, v10, v11 op_sel:[0,0,1]
	v_lshl_add_u64 v[6:7], s[14:15], 0, v[6:7]
	v_lshl_add_u64 v[6:7], v[6:7], 0, v[2:3]
	global_store_dwordx2 v[6:7], v[12:13], off
	global_store_dwordx2 v[6:7], v[14:15], off offset:128
	v_pk_fma_f32 v[8:9], v[78:79], s[18:19], v[26:27] op_sel_hi:[1,0,1]
	v_pk_fma_f32 v[10:11], v[74:75], s[18:19], v[22:23] op_sel_hi:[1,0,1]
	v_cvt_pk_fp8_f32 v12, v8, v9
	v_cvt_pk_fp8_f32 v13, v10, v11
	v_pk_fma_f32 v[8:9], v[80:81], s[18:19], v[28:29] op_sel_hi:[1,0,1]
	v_pk_fma_f32 v[10:11], v[76:77], s[18:19], v[24:25] op_sel_hi:[1,0,1]
	v_cvt_pk_fp8_f32 v12, v8, v9 op_sel:[0,0,1]
	v_cvt_pk_fp8_f32 v13, v10, v11 op_sel:[0,0,1]
	v_pk_fma_f32 v[8:9], v[70:71], s[18:19], v[30:31] op_sel_hi:[1,0,1]
	v_pk_fma_f32 v[10:11], v[66:67], s[18:19], v[18:19] op_sel_hi:[1,0,1]
	v_cvt_pk_fp8_f32 v14, v8, v9
	v_cvt_pk_fp8_f32 v15, v10, v11
	v_add_u32_e32 v6, 0x90, v4
	v_ashrrev_i32_e32 v7, 31, v6
	v_pk_fma_f32 v[8:9], v[72:73], s[18:19], v[32:33] op_sel_hi:[1,0,1]
	v_pk_fma_f32 v[10:11], v[68:69], s[18:19], v[20:21] op_sel_hi:[1,0,1]
	v_lshlrev_b64 v[6:7], 11, v[6:7]
	v_cvt_pk_fp8_f32 v14, v8, v9 op_sel:[0,0,1]
	v_cvt_pk_fp8_f32 v15, v10, v11 op_sel:[0,0,1]
	v_lshl_add_u64 v[6:7], s[14:15], 0, v[6:7]
	v_lshl_add_u64 v[6:7], v[6:7], 0, v[2:3]
	global_store_dwordx2 v[6:7], v[12:13], off
	global_store_dwordx2 v[6:7], v[14:15], off offset:128
	v_pk_fma_f32 v[8:9], v[62:63], s[18:19], v[26:27] op_sel_hi:[1,0,1]
	v_pk_fma_f32 v[10:11], v[58:59], s[18:19], v[22:23] op_sel_hi:[1,0,1]
	v_cvt_pk_fp8_f32 v12, v8, v9
	v_cvt_pk_fp8_f32 v13, v10, v11
	v_pk_fma_f32 v[8:9], v[64:65], s[18:19], v[28:29] op_sel_hi:[1,0,1]
	v_pk_fma_f32 v[10:11], v[60:61], s[18:19], v[24:25] op_sel_hi:[1,0,1]
	v_cvt_pk_fp8_f32 v12, v8, v9 op_sel:[0,0,1]
	v_cvt_pk_fp8_f32 v13, v10, v11 op_sel:[0,0,1]
	v_pk_fma_f32 v[8:9], v[54:55], s[18:19], v[30:31] op_sel_hi:[1,0,1]
	v_pk_fma_f32 v[10:11], v[50:51], s[18:19], v[18:19] op_sel_hi:[1,0,1]
	v_cvt_pk_fp8_f32 v14, v8, v9
	v_cvt_pk_fp8_f32 v15, v10, v11
	v_add_u32_e32 v6, 0xa0, v4
	v_ashrrev_i32_e32 v7, 31, v6
	v_pk_fma_f32 v[8:9], v[56:57], s[18:19], v[32:33] op_sel_hi:[1,0,1]
	v_pk_fma_f32 v[10:11], v[52:53], s[18:19], v[20:21] op_sel_hi:[1,0,1]
	v_lshlrev_b64 v[6:7], 11, v[6:7]
	v_cvt_pk_fp8_f32 v14, v8, v9 op_sel:[0,0,1]
	v_cvt_pk_fp8_f32 v15, v10, v11 op_sel:[0,0,1]
	v_lshl_add_u64 v[6:7], s[14:15], 0, v[6:7]
	v_lshl_add_u64 v[6:7], v[6:7], 0, v[2:3]
	global_store_dwordx2 v[6:7], v[12:13], off
	global_store_dwordx2 v[6:7], v[14:15], off offset:128
	v_pk_fma_f32 v[6:7], v[46:47], s[18:19], v[26:27] op_sel_hi:[1,0,1]
	v_pk_fma_f32 v[8:9], v[42:43], s[18:19], v[22:23] op_sel_hi:[1,0,1]
	v_cvt_pk_fp8_f32 v10, v6, v7
	v_cvt_pk_fp8_f32 v11, v8, v9
	v_pk_fma_f32 v[6:7], v[48:49], s[18:19], v[28:29] op_sel_hi:[1,0,1]
	v_pk_fma_f32 v[8:9], v[44:45], s[18:19], v[24:25] op_sel_hi:[1,0,1]
	v_cvt_pk_fp8_f32 v10, v6, v7 op_sel:[0,0,1]
	v_cvt_pk_fp8_f32 v11, v8, v9 op_sel:[0,0,1]
	v_pk_fma_f32 v[6:7], v[38:39], s[18:19], v[30:31] op_sel_hi:[1,0,1]
	v_pk_fma_f32 v[8:9], v[34:35], s[18:19], v[18:19] op_sel_hi:[1,0,1]
	v_cvt_pk_fp8_f32 v12, v6, v7
	v_cvt_pk_fp8_f32 v13, v8, v9
	v_add_u32_e32 v4, 0xb0, v4
	v_ashrrev_i32_e32 v5, 31, v4
	v_pk_fma_f32 v[6:7], v[40:41], s[18:19], v[32:33] op_sel_hi:[1,0,1]
	v_pk_fma_f32 v[8:9], v[36:37], s[18:19], v[20:21] op_sel_hi:[1,0,1]
	v_lshlrev_b64 v[4:5], 11, v[4:5]
	v_cvt_pk_fp8_f32 v12, v6, v7 op_sel:[0,0,1]
	v_cvt_pk_fp8_f32 v13, v8, v9 op_sel:[0,0,1]
	v_lshl_add_u64 v[4:5], s[14:15], 0, v[4:5]
	v_lshl_add_u64 v[2:3], v[4:5], 0, v[2:3]
	s_and_b64 vcc, exec, s[16:17]
	s_cbranch_vccz .Lhyb_p6
	s_barrier
.Lhyb_p6:
	s_andn2_b64 vcc, exec, s[0:1]
	s_mov_b64 s[0:1], -1
	global_store_dwordx2 v[2:3], v[10:11], off
	global_store_dwordx2 v[2:3], v[12:13], off offset:128
	s_cbranch_vccnz .LBB0_1001
	s_andn2_b64 vcc, exec, s[12:13]
	s_cbranch_vccnz .LBB0_1000
	s_barrier
	s_branch .LBB0_1000
